# v42: v40 + grid barrier: every workgroup waits on the cross-XCD arrival counter reaching the round total instead of the relayed generation words (TOPGEN then per-XCD XGEN); leaders' write-back still p
# speedup vs baseline: 1.0039x; 1.0039x over previous
; __device__ __forceinline__ unsigned xb_ld(unsigned* p)              { return __hip_atomic_load(p, __ATOMIC_RELAXED, __HIP_MEMORY_SCOPE_AGENT); }
; __device__ __forceinline__ unsigned xb_add(unsigned* p, unsigned v) { return __hip_atomic_fetch_add(p, v, __ATOMIC_RELAXED, __HIP_MEMORY_SCOPE_AGENT); }
; #define XB_SPIN(cond, bar) do { unsigned _sp = 0; while (cond) { __builtin_amdgcn_s_sleep(1); \
;     if ((++_sp & 255u) == 0u) { if (xb_ld(&(bar)[XB_TMO])) break; if (_sp > XB_SPIN_CAP) { atomicAdd(&(bar)[XB_TMO], 1u); break; } } } } while (0)
; __device__ __forceinline__ void xcd_barrier(const XcdBarrier& b) {
;     ...
;         const unsigned old = xb_add(&bar[XB_XSUB(b.x)], 1u);
;         const unsigned gen = old / nloc;
;         if (old + 1u == (gen + 1u) * nloc) {
;     ...
;         } else {
;             XB_SPIN(xb_ld(&bar[XB_XGEN(b.x)]) == gen, bar);
.LBB0_68:
	s_or_b64 exec, exec, s[8:9]
	v_cvt_f32_u32_e32 v5, v3
	s_waitcnt vmcnt(0)
	v_readfirstlane_b32 s6, v4
	v_sub_u32_e32 v4, 0, v3
	v_rcp_iflag_f32_e32 v5, v5
	v_add_u32_e32 v6, s6, v2
	v_mul_f32_e32 v5, 0x4f7ffffe, v5
	v_cvt_u32_f32_e32 v5, v5
	v_mul_lo_u32 v2, v4, v5
	v_mul_hi_u32 v2, v5, v2
	v_add_u32_e32 v2, v5, v2
	v_mul_hi_u32 v2, v6, v2
	v_mul_lo_u32 v4, v2, v3
	v_sub_u32_e32 v4, v6, v4
	v_add_u32_e32 v5, 1, v2
	v_cmp_ge_u32_e32 vcc, v4, v3
	s_nop 1
	v_cndmask_b32_e32 v2, v2, v5, vcc
	v_sub_u32_e32 v5, v4, v3
	v_cndmask_b32_e32 v4, v4, v5, vcc
	v_add_u32_e32 v5, 1, v2
	v_cmp_ge_u32_e32 vcc, v4, v3
	v_add_u32_e32 v4, 1, v6
	s_nop 0
	v_cndmask_b32_e32 v2, v2, v5, vcc
	v_mul_lo_u32 v5, v3, v2
	v_add_u32_e32 v3, v5, v3
	v_cmp_ne_u32_e32 vcc, v4, v3
	s_and_saveexec_b64 s[6:7], vcc
	s_xor_b64 s[6:7], exec, s[6:7]
	s_cbranch_execz .LBB0_82
	s_waitcnt lgkmcnt(0)
	v_add_u32_e32 v6, 1, v2
	v_mul_lo_u32 v6, v6, v1
	s_add_u32 s98, s88, 0x7400
	s_addc_u32 s99, s89, 0
	v_mov_b32_e32 v1, 0
	global_load_dword v1, v1, s[98:99] sc1
	s_add_u32 s12, s4, 0x2400
	s_addc_u32 s13, s5, 0
	s_waitcnt vmcnt(0)
	v_cmp_lt_u32_e32 vcc, v1, v6
	s_and_saveexec_b64 s[8:9], vcc
	s_cbranch_execz .LBB0_81
	s_add_u32 s10, s88, 0x4200
	s_addc_u32 s11, s89, 0
	s_mov_b32 s24, 1
	s_mov_b64 s[14:15], 0
	v_mov_b32_e32 v1, 0
	s_branch .LBB0_72

; __device__ __forceinline__ unsigned xb_ld(unsigned* p)              { return __hip_atomic_load(p, __ATOMIC_RELAXED, __HIP_MEMORY_SCOPE_AGENT); }
; #define XB_SPIN(cond, bar) do { unsigned _sp = 0; while (cond) { __builtin_amdgcn_s_sleep(1); \
;     if ((++_sp & 255u) == 0u) { if (xb_ld(&(bar)[XB_TMO])) break; if (_sp > XB_SPIN_CAP) { atomicAdd(&(bar)[XB_TMO], 1u); break; } } } } while (0)
; __device__ __forceinline__ void xcd_barrier(const XcdBarrier& b) {
;     ...
;             XB_SPIN(xb_ld(&bar[XB_XGEN(b.x)]) == gen, bar);
.LBB0_76:
	global_load_dword v3, v1, s[98:99] sc1
	s_add_i32 s24, s24, 1
	s_mov_b64 s[20:21], -1
	s_waitcnt vmcnt(0)
	v_cmp_ge_u32_e32 vcc, v3, v6
	s_orn2_b64 s[18:19], vcc, exec
	s_branch .LBB0_71

; __device__ __forceinline__ unsigned xb_ld(unsigned* p)              { return __hip_atomic_load(p, __ATOMIC_RELAXED, __HIP_MEMORY_SCOPE_AGENT); }
; __device__ __forceinline__ unsigned xb_add(unsigned* p, unsigned v) { return __hip_atomic_fetch_add(p, v, __ATOMIC_RELAXED, __HIP_MEMORY_SCOPE_AGENT); }
; #define XB_SPIN(cond, bar) do { unsigned _sp = 0; while (cond) { __builtin_amdgcn_s_sleep(1); \
;     if ((++_sp & 255u) == 0u) { if (xb_ld(&(bar)[XB_TMO])) break; if (_sp > XB_SPIN_CAP) { atomicAdd(&(bar)[XB_TMO], 1u); break; } } } } while (0)
; __device__ __forceinline__ void xcd_barrier(const XcdBarrier& b) {
;     ...
;             const unsigned og = xb_add(&bar[XB_TOP], 1u);
;             const unsigned tg = og / nx;
;             if (og + 1u == (tg + 1u) * nx) xb_add(&bar[XB_TOPGEN], 1u);
;             else XB_SPIN(xb_ld(&bar[XB_TOPGEN]) == tg, bar);
.LBB0_85:
	s_or_b64 exec, exec, s[8:9]
	v_cvt_f32_u32_e32 v4, v1
	s_waitcnt vmcnt(0)
	v_readfirstlane_b32 s6, v3
	s_add_u32 s8, s88, 0x7500
	s_addc_u32 s9, s89, 0
	v_rcp_iflag_f32_e32 v4, v4
	v_add_u32_e32 v2, s6, v2
	v_add_u32_e32 v5, 1, v2
	s_mov_b64 s[10:11], -1
	v_mul_f32_e32 v3, 0x4f7ffffe, v4
	v_cvt_u32_f32_e32 v3, v3
	v_sub_u32_e32 v4, 0, v1
	v_mul_lo_u32 v4, v4, v3
	v_mul_hi_u32 v4, v3, v4
	v_add_u32_e32 v3, v3, v4
	v_mul_hi_u32 v3, v2, v3
	v_mul_lo_u32 v4, v3, v1
	v_sub_u32_e32 v2, v2, v4
	v_add_u32_e32 v6, 1, v3
	v_cmp_ge_u32_e32 vcc, v2, v1
	v_sub_u32_e32 v4, v2, v1
	s_nop 0
	v_cndmask_b32_e32 v3, v3, v6, vcc
	v_cndmask_b32_e32 v2, v2, v4, vcc
	v_add_u32_e32 v4, 1, v3
	v_cmp_ge_u32_e32 vcc, v2, v1
	s_nop 1
	v_cndmask_b32_e32 v4, v3, v4, vcc
	v_mul_lo_u32 v2, v1, v4
	v_add_u32_e32 v1, v2, v1
	v_cmp_ne_u32_e32 vcc, v5, v1
	v_mov_b64_e32 v[2:3], s[8:9]
	s_and_saveexec_b64 s[6:7], vcc
	s_cbranch_execz .LBB0_97
	v_mov_b32_e32 v6, v1
	s_add_u32 s98, s88, 0x7400
	s_addc_u32 s99, s89, 0
	v_mov_b32_e32 v1, 0
	global_load_dword v2, v1, s[98:99] sc1
	s_mov_b64 s[14:15], 0
	s_waitcnt vmcnt(0)
	v_cmp_lt_u32_e32 vcc, v2, v6
	s_and_saveexec_b64 s[12:13], vcc
	s_cbranch_execz .LBB0_96
	s_add_u32 s10, s88, 0x4200
	s_addc_u32 s11, s89, 0
	s_mov_b32 s24, 1
	s_branch .LBB0_89

; __device__ __forceinline__ unsigned xb_ld(unsigned* p)              { return __hip_atomic_load(p, __ATOMIC_RELAXED, __HIP_MEMORY_SCOPE_AGENT); }
; #define XB_SPIN(cond, bar) do { unsigned _sp = 0; while (cond) { __builtin_amdgcn_s_sleep(1); \
;     if ((++_sp & 255u) == 0u) { if (xb_ld(&(bar)[XB_TMO])) break; if (_sp > XB_SPIN_CAP) { atomicAdd(&(bar)[XB_TMO], 1u); break; } } } } while (0)
; __device__ __forceinline__ void xcd_barrier(const XcdBarrier& b) {
;     ...
;             else XB_SPIN(xb_ld(&bar[XB_TOPGEN]) == tg, bar);
.LBB0_93:
	global_load_dword v2, v1, s[98:99] sc1
	s_add_i32 s24, s24, 1
	s_mov_b64 s[18:19], -1
	s_waitcnt vmcnt(0)
	v_cmp_ge_u32_e32 vcc, v2, v6
	s_orn2_b64 s[22:23], vcc, exec
	s_branch .LBB0_88

; __device__ __forceinline__ unsigned xb_add(unsigned* p, unsigned v) { return __hip_atomic_fetch_add(p, v, __ATOMIC_RELAXED, __HIP_MEMORY_SCOPE_AGENT); }
; __device__ __forceinline__ void xcd_barrier(const XcdBarrier& b) {
;     ...
;             __builtin_amdgcn_fence(__ATOMIC_ACQUIRE, "agent");
;             xb_add(&bar[XB_XGEN(b.x)], 1u);
;             asm volatile("s_waitcnt vmcnt(0)" ::: "memory");
.LBB0_99:
	s_or_b64 exec, exec, s[6:7]
	s_mov_b64 s[6:7], exec
	v_mbcnt_lo_u32_b32 v1, s6, 0
	v_mbcnt_hi_u32_b32 v1, s7, v1
	v_cmp_eq_u32_e32 vcc, 0, v1
	s_waitcnt vmcnt(0)
	buffer_inv sc1
	s_and_saveexec_b64 s[8:9], vcc
	s_cbranch_execz .LBB0_101
	s_bcnt1_i32_b64 s6, s[6:7]
	v_mov_b32_e32 v1, 0x2000
	v_mov_b32_e32 v2, s6
.LBB0_101:
	s_or_b64 exec, exec, s[8:9]
	s_waitcnt vmcnt(0)

; __device__ __forceinline__ unsigned xb_add(unsigned* p, unsigned v) { return __hip_atomic_fetch_add(p, v, __ATOMIC_RELAXED, __HIP_MEMORY_SCOPE_AGENT); }
; __device__ __forceinline__ void xcd_barrier(const XcdBarrier& b) {
;     ...
;             __builtin_amdgcn_fence(__ATOMIC_ACQUIRE, "agent");
;             xb_add(&bar[XB_XGEN(b.x)], 1u);
;             asm volatile("s_waitcnt vmcnt(0)" ::: "memory");
.LBB0_160:
	s_or_b64 exec, exec, s[6:7]
	s_mov_b64 s[6:7], exec
	v_mbcnt_lo_u32_b32 v1, s6, 0
	v_mbcnt_hi_u32_b32 v1, s7, v1
	v_cmp_eq_u32_e32 vcc, 0, v1
	s_waitcnt vmcnt(0)
	buffer_inv sc1
	s_and_saveexec_b64 s[8:9], vcc
	s_cbranch_execz .LBB0_162
	s_bcnt1_i32_b64 s6, s[6:7]
	v_mov_b32_e32 v1, 0x2000
	v_mov_b32_e32 v2, s6
.LBB0_162:
	s_or_b64 exec, exec, s[8:9]
	s_waitcnt vmcnt(0)

; __device__ __forceinline__ unsigned xb_add(unsigned* p, unsigned v) { return __hip_atomic_fetch_add(p, v, __ATOMIC_RELAXED, __HIP_MEMORY_SCOPE_AGENT); }
; __device__ __forceinline__ void xcd_barrier(const XcdBarrier& b) {
;     ...
;             __builtin_amdgcn_fence(__ATOMIC_ACQUIRE, "agent");
;             xb_add(&bar[XB_XGEN(b.x)], 1u);
;             asm volatile("s_waitcnt vmcnt(0)" ::: "memory");
.LBB0_218:
	s_or_b64 exec, exec, s[6:7]
	s_mov_b64 s[6:7], exec
	v_mbcnt_lo_u32_b32 v1, s6, 0
	v_mbcnt_hi_u32_b32 v1, s7, v1
	v_cmp_eq_u32_e32 vcc, 0, v1
	s_waitcnt vmcnt(0)
	buffer_inv sc1
	s_and_saveexec_b64 s[8:9], vcc
	s_cbranch_execz .LBB0_220
	s_bcnt1_i32_b64 s6, s[6:7]
	v_mov_b32_e32 v1, 0x2000
	v_mov_b32_e32 v2, s6
.LBB0_220:
	s_or_b64 exec, exec, s[8:9]
	s_waitcnt vmcnt(0)

; __device__ __forceinline__ unsigned xb_add(unsigned* p, unsigned v) { return __hip_atomic_fetch_add(p, v, __ATOMIC_RELAXED, __HIP_MEMORY_SCOPE_AGENT); }
; __device__ __forceinline__ void xcd_barrier(const XcdBarrier& b) {
;     ...
;             __builtin_amdgcn_fence(__ATOMIC_ACQUIRE, "agent");
;             xb_add(&bar[XB_XGEN(b.x)], 1u);
;             asm volatile("s_waitcnt vmcnt(0)" ::: "memory");
.LBB0_326:
	s_or_b64 exec, exec, s[6:7]
	s_mov_b64 s[6:7], exec
	v_mbcnt_lo_u32_b32 v1, s6, 0
	v_mbcnt_hi_u32_b32 v1, s7, v1
	v_cmp_eq_u32_e32 vcc, 0, v1
	s_waitcnt vmcnt(0)
	buffer_inv sc1
	s_and_saveexec_b64 s[8:9], vcc
	s_cbranch_execz .LBB0_328
	s_bcnt1_i32_b64 s6, s[6:7]
	v_mov_b32_e32 v1, 0x2000
	v_mov_b32_e32 v2, s6
.LBB0_328:
	s_or_b64 exec, exec, s[8:9]
	s_waitcnt vmcnt(0)

; __device__ __forceinline__ unsigned xb_add(unsigned* p, unsigned v) { return __hip_atomic_fetch_add(p, v, __ATOMIC_RELAXED, __HIP_MEMORY_SCOPE_AGENT); }
; __device__ __forceinline__ void xcd_barrier(const XcdBarrier& b) {
;     ...
;             __builtin_amdgcn_fence(__ATOMIC_ACQUIRE, "agent");
;             xb_add(&bar[XB_XGEN(b.x)], 1u);
;             asm volatile("s_waitcnt vmcnt(0)" ::: "memory");
.LBB0_525:
	s_or_b64 exec, exec, s[6:7]
	s_mov_b64 s[6:7], exec
	v_mbcnt_lo_u32_b32 v1, s6, 0
	v_mbcnt_hi_u32_b32 v1, s7, v1
	v_cmp_eq_u32_e32 vcc, 0, v1
	s_waitcnt vmcnt(0)
	buffer_inv sc1
	s_and_saveexec_b64 s[8:9], vcc
	s_cbranch_execz .LBB0_527
	s_bcnt1_i32_b64 s6, s[6:7]
	v_mov_b32_e32 v1, 0x2000
	v_mov_b32_e32 v2, s6
.LBB0_527:
	s_or_b64 exec, exec, s[8:9]
	s_waitcnt vmcnt(0)

; __device__ __forceinline__ unsigned xb_add(unsigned* p, unsigned v) { return __hip_atomic_fetch_add(p, v, __ATOMIC_RELAXED, __HIP_MEMORY_SCOPE_AGENT); }
; __device__ __forceinline__ void xcd_barrier(const XcdBarrier& b) {
;     ...
;             __builtin_amdgcn_fence(__ATOMIC_ACQUIRE, "agent");
;             xb_add(&bar[XB_XGEN(b.x)], 1u);
;             asm volatile("s_waitcnt vmcnt(0)" ::: "memory");
.LBB0_934:
	s_or_b64 exec, exec, s[6:7]
	s_mov_b64 s[6:7], exec
	v_mbcnt_lo_u32_b32 v1, s6, 0
	v_mbcnt_hi_u32_b32 v1, s7, v1
	v_cmp_eq_u32_e32 vcc, 0, v1
	s_waitcnt vmcnt(0)
	buffer_inv sc1
	s_and_saveexec_b64 s[8:9], vcc
	s_cbranch_execz .LBB0_936
	s_bcnt1_i32_b64 s6, s[6:7]
	v_mov_b32_e32 v1, 0x2000
	v_mov_b32_e32 v2, s6
.LBB0_936:
	s_or_b64 exec, exec, s[8:9]
	s_waitcnt vmcnt(0)

; __device__ __forceinline__ unsigned xb_add(unsigned* p, unsigned v) { return __hip_atomic_fetch_add(p, v, __ATOMIC_RELAXED, __HIP_MEMORY_SCOPE_AGENT); }
; __device__ __forceinline__ void xcd_barrier(const XcdBarrier& b) {
;     ...
;             __builtin_amdgcn_fence(__ATOMIC_ACQUIRE, "agent");
;             xb_add(&bar[XB_XGEN(b.x)], 1u);
;             asm volatile("s_waitcnt vmcnt(0)" ::: "memory");
.LBB0_1025:
	s_or_b64 exec, exec, s[6:7]
	s_mov_b64 s[6:7], exec
	v_mbcnt_lo_u32_b32 v1, s6, 0
	v_mbcnt_hi_u32_b32 v1, s7, v1
	v_cmp_eq_u32_e32 vcc, 0, v1
	s_waitcnt vmcnt(0)
	buffer_inv sc1
	s_and_saveexec_b64 s[8:9], vcc
	s_cbranch_execz .LBB0_1027
	s_bcnt1_i32_b64 s6, s[6:7]
	v_mov_b32_e32 v1, 0x2000
	v_mov_b32_e32 v2, s6
.LBB0_1027:
	s_or_b64 exec, exec, s[8:9]
	s_waitcnt vmcnt(0)

; __device__ __forceinline__ unsigned xb_add(unsigned* p, unsigned v) { return __hip_atomic_fetch_add(p, v, __ATOMIC_RELAXED, __HIP_MEMORY_SCOPE_AGENT); }
; __device__ __forceinline__ void xcd_barrier(const XcdBarrier& b) {
;     ...
;             __builtin_amdgcn_fence(__ATOMIC_ACQUIRE, "agent");
;             xb_add(&bar[XB_XGEN(b.x)], 1u);
;             asm volatile("s_waitcnt vmcnt(0)" ::: "memory");
.LBB0_1106:
	s_or_b64 exec, exec, s[6:7]
	s_mov_b64 s[6:7], exec
	v_mbcnt_lo_u32_b32 v1, s6, 0
	v_mbcnt_hi_u32_b32 v1, s7, v1
	v_cmp_eq_u32_e32 vcc, 0, v1
	s_waitcnt vmcnt(0)
	buffer_inv sc1
	s_and_saveexec_b64 s[8:9], vcc
	s_cbranch_execz .LBB0_1108
	s_bcnt1_i32_b64 s6, s[6:7]
	v_mov_b32_e32 v1, 0x2000
	v_mov_b32_e32 v2, s6
.LBB0_1108:
	s_or_b64 exec, exec, s[8:9]
	s_waitcnt vmcnt(0)

; __device__ __forceinline__ unsigned xb_add(unsigned* p, unsigned v) { return __hip_atomic_fetch_add(p, v, __ATOMIC_RELAXED, __HIP_MEMORY_SCOPE_AGENT); }
; __device__ __forceinline__ void xcd_barrier(const XcdBarrier& b) {
;     ...
;             __builtin_amdgcn_fence(__ATOMIC_ACQUIRE, "agent");
;             xb_add(&bar[XB_XGEN(b.x)], 1u);
;             asm volatile("s_waitcnt vmcnt(0)" ::: "memory");
.LBB0_1185:
	s_or_b64 exec, exec, s[6:7]
	s_mov_b64 s[6:7], exec
	v_mbcnt_lo_u32_b32 v1, s6, 0
	v_mbcnt_hi_u32_b32 v1, s7, v1
	v_cmp_eq_u32_e32 vcc, 0, v1
	s_waitcnt vmcnt(0)
	buffer_inv sc1
	s_and_saveexec_b64 s[8:9], vcc
	s_cbranch_execz .LBB0_1187
	s_bcnt1_i32_b64 s6, s[6:7]
	v_mov_b32_e32 v1, 0x2000
	v_mov_b32_e32 v2, s6
.LBB0_1187:
	s_or_b64 exec, exec, s[8:9]
	s_waitcnt vmcnt(0)

; __device__ __forceinline__ unsigned xb_add(unsigned* p, unsigned v) { return __hip_atomic_fetch_add(p, v, __ATOMIC_RELAXED, __HIP_MEMORY_SCOPE_AGENT); }
; __device__ __forceinline__ void xcd_barrier(const XcdBarrier& b) {
;     ...
;             __builtin_amdgcn_fence(__ATOMIC_ACQUIRE, "agent");
;             xb_add(&bar[XB_XGEN(b.x)], 1u);
;             asm volatile("s_waitcnt vmcnt(0)" ::: "memory");
.LBB0_1293:
	s_or_b64 exec, exec, s[6:7]
	s_mov_b64 s[6:7], exec
	v_mbcnt_lo_u32_b32 v1, s6, 0
	v_mbcnt_hi_u32_b32 v1, s7, v1
	v_cmp_eq_u32_e32 vcc, 0, v1
	s_waitcnt vmcnt(0)
	buffer_inv sc1
	s_and_saveexec_b64 s[8:9], vcc
	s_cbranch_execz .LBB0_1295
	s_bcnt1_i32_b64 s6, s[6:7]
	v_mov_b32_e32 v1, 0x2000
	v_mov_b32_e32 v2, s6
.LBB0_1295:
	s_or_b64 exec, exec, s[8:9]
	s_waitcnt vmcnt(0)

; __device__ __forceinline__ unsigned xb_ld(unsigned* p)              { return __hip_atomic_load(p, __ATOMIC_RELAXED, __HIP_MEMORY_SCOPE_AGENT); }
; __device__ __forceinline__ unsigned xb_add(unsigned* p, unsigned v) { return __hip_atomic_fetch_add(p, v, __ATOMIC_RELAXED, __HIP_MEMORY_SCOPE_AGENT); }
; #define XB_SPIN(cond, bar) do { unsigned _sp = 0; while (cond) { __builtin_amdgcn_s_sleep(1); \
;     if ((++_sp & 255u) == 0u) { if (xb_ld(&(bar)[XB_TMO])) break; if (_sp > XB_SPIN_CAP) { atomicAdd(&(bar)[XB_TMO], 1u); break; } } } } while (0)
; __device__ __forceinline__ void xcd_barrier(const XcdBarrier& b) {
;     ...
;         const unsigned old = xb_add(&bar[XB_XSUB(b.x)], 1u);
;         const unsigned gen = old / nloc;
;         if (old + 1u == (gen + 1u) * nloc) {
;     ...
;         } else {
;             XB_SPIN(xb_ld(&bar[XB_XGEN(b.x)]) == gen, bar);
.LBB0_1383:
	s_or_b64 exec, exec, s[8:9]
	v_cvt_f32_u32_e32 v5, v3
	s_waitcnt vmcnt(0)
	v_readfirstlane_b32 s6, v4
	v_sub_u32_e32 v4, 0, v3
	v_rcp_iflag_f32_e32 v5, v5
	v_add_u32_e32 v6, s6, v2
	v_mul_f32_e32 v5, 0x4f7ffffe, v5
	v_cvt_u32_f32_e32 v5, v5
	v_mul_lo_u32 v2, v4, v5
	v_mul_hi_u32 v2, v5, v2
	v_add_u32_e32 v2, v5, v2
	v_mul_hi_u32 v2, v6, v2
	v_mul_lo_u32 v4, v2, v3
	v_sub_u32_e32 v4, v6, v4
	v_add_u32_e32 v5, 1, v2
	v_cmp_ge_u32_e32 vcc, v4, v3
	s_nop 1
	v_cndmask_b32_e32 v2, v2, v5, vcc
	v_sub_u32_e32 v5, v4, v3
	v_cndmask_b32_e32 v4, v4, v5, vcc
	v_add_u32_e32 v5, 1, v2
	v_cmp_ge_u32_e32 vcc, v4, v3
	v_add_u32_e32 v4, 1, v6
	s_nop 0
	v_cndmask_b32_e32 v2, v2, v5, vcc
	v_mul_lo_u32 v5, v3, v2
	v_add_u32_e32 v3, v5, v3
	v_cmp_ne_u32_e32 vcc, v4, v3
	s_and_saveexec_b64 s[6:7], vcc
	s_xor_b64 s[6:7], exec, s[6:7]
	s_cbranch_execz .LBB0_1397
	s_waitcnt lgkmcnt(0)
	v_add_u32_e32 v6, 1, v2
	v_mul_lo_u32 v6, v6, v1
	s_add_u32 s98, s88, 0x7400
	s_addc_u32 s99, s89, 0
	v_mov_b32_e32 v1, 0
	global_load_dword v1, v1, s[98:99] sc1
	s_add_u32 s12, s4, 0x2400
	s_addc_u32 s13, s5, 0
	s_waitcnt vmcnt(0)
	v_cmp_lt_u32_e32 vcc, v1, v6
	s_and_saveexec_b64 s[8:9], vcc
	s_cbranch_execz .LBB0_1396
	s_add_u32 s10, s88, 0x4200
	s_addc_u32 s11, s89, 0
	s_mov_b32 s26, 1
	s_mov_b64 s[16:17], 0
	v_mov_b32_e32 v1, 0
	s_branch .LBB0_1387

; __device__ __forceinline__ unsigned xb_ld(unsigned* p)              { return __hip_atomic_load(p, __ATOMIC_RELAXED, __HIP_MEMORY_SCOPE_AGENT); }
; #define XB_SPIN(cond, bar) do { unsigned _sp = 0; while (cond) { __builtin_amdgcn_s_sleep(1); \
;     if ((++_sp & 255u) == 0u) { if (xb_ld(&(bar)[XB_TMO])) break; if (_sp > XB_SPIN_CAP) { atomicAdd(&(bar)[XB_TMO], 1u); break; } } } } while (0)
; __device__ __forceinline__ void xcd_barrier(const XcdBarrier& b) {
;     ...
;             XB_SPIN(xb_ld(&bar[XB_XGEN(b.x)]) == gen, bar);
.LBB0_1391:
	global_load_dword v3, v1, s[98:99] sc1
	s_add_i32 s26, s26, 1
	s_mov_b64 s[22:23], -1
	s_waitcnt vmcnt(0)
	v_cmp_ge_u32_e32 vcc, v3, v6
	s_orn2_b64 s[20:21], vcc, exec
	s_branch .LBB0_1386

; __device__ __forceinline__ unsigned xb_ld(unsigned* p)              { return __hip_atomic_load(p, __ATOMIC_RELAXED, __HIP_MEMORY_SCOPE_AGENT); }
; __device__ __forceinline__ unsigned xb_add(unsigned* p, unsigned v) { return __hip_atomic_fetch_add(p, v, __ATOMIC_RELAXED, __HIP_MEMORY_SCOPE_AGENT); }
; #define XB_SPIN(cond, bar) do { unsigned _sp = 0; while (cond) { __builtin_amdgcn_s_sleep(1); \
;     if ((++_sp & 255u) == 0u) { if (xb_ld(&(bar)[XB_TMO])) break; if (_sp > XB_SPIN_CAP) { atomicAdd(&(bar)[XB_TMO], 1u); break; } } } } while (0)
; __device__ __forceinline__ void xcd_barrier(const XcdBarrier& b) {
;     ...
;             const unsigned og = xb_add(&bar[XB_TOP], 1u);
;             const unsigned tg = og / nx;
;             if (og + 1u == (tg + 1u) * nx) xb_add(&bar[XB_TOPGEN], 1u);
;             else XB_SPIN(xb_ld(&bar[XB_TOPGEN]) == tg, bar);
.LBB0_1400:
	s_or_b64 exec, exec, s[8:9]
	v_cvt_f32_u32_e32 v4, v1
	s_waitcnt vmcnt(0)
	v_readfirstlane_b32 s6, v3
	s_add_u32 s8, s88, 0x7500
	s_addc_u32 s9, s89, 0
	v_rcp_iflag_f32_e32 v4, v4
	v_add_u32_e32 v2, s6, v2
	v_add_u32_e32 v5, 1, v2
	s_mov_b64 s[10:11], -1
	v_mul_f32_e32 v3, 0x4f7ffffe, v4
	v_cvt_u32_f32_e32 v3, v3
	v_sub_u32_e32 v4, 0, v1
	v_mul_lo_u32 v4, v4, v3
	v_mul_hi_u32 v4, v3, v4
	v_add_u32_e32 v3, v3, v4
	v_mul_hi_u32 v3, v2, v3
	v_mul_lo_u32 v4, v3, v1
	v_sub_u32_e32 v2, v2, v4
	v_add_u32_e32 v6, 1, v3
	v_cmp_ge_u32_e32 vcc, v2, v1
	v_sub_u32_e32 v4, v2, v1
	s_nop 0
	v_cndmask_b32_e32 v3, v3, v6, vcc
	v_cndmask_b32_e32 v2, v2, v4, vcc
	v_add_u32_e32 v4, 1, v3
	v_cmp_ge_u32_e32 vcc, v2, v1
	s_nop 1
	v_cndmask_b32_e32 v4, v3, v4, vcc
	v_mul_lo_u32 v2, v1, v4
	v_add_u32_e32 v1, v2, v1
	v_cmp_ne_u32_e32 vcc, v5, v1
	v_mov_b64_e32 v[2:3], s[8:9]
	s_and_saveexec_b64 s[6:7], vcc
	s_cbranch_execz .LBB0_1412
	v_mov_b32_e32 v6, v1
	s_add_u32 s98, s88, 0x7400
	s_addc_u32 s99, s89, 0
	v_mov_b32_e32 v1, 0
	global_load_dword v2, v1, s[98:99] sc1
	s_mov_b64 s[16:17], 0
	s_waitcnt vmcnt(0)
	v_cmp_lt_u32_e32 vcc, v2, v6
	s_and_saveexec_b64 s[12:13], vcc
	s_cbranch_execz .LBB0_1411
	s_add_u32 s10, s88, 0x4200
	s_addc_u32 s11, s89, 0
	s_mov_b32 s26, 1
	s_branch .LBB0_1404

; __device__ __forceinline__ unsigned xb_ld(unsigned* p)              { return __hip_atomic_load(p, __ATOMIC_RELAXED, __HIP_MEMORY_SCOPE_AGENT); }
; #define XB_SPIN(cond, bar) do { unsigned _sp = 0; while (cond) { __builtin_amdgcn_s_sleep(1); \
;     if ((++_sp & 255u) == 0u) { if (xb_ld(&(bar)[XB_TMO])) break; if (_sp > XB_SPIN_CAP) { atomicAdd(&(bar)[XB_TMO], 1u); break; } } } } while (0)
; __device__ __forceinline__ void xcd_barrier(const XcdBarrier& b) {
;     ...
;             else XB_SPIN(xb_ld(&bar[XB_TOPGEN]) == tg, bar);
.LBB0_1408:
	global_load_dword v2, v1, s[98:99] sc1
	s_add_i32 s26, s26, 1
	s_mov_b64 s[20:21], -1
	s_waitcnt vmcnt(0)
	v_cmp_ge_u32_e32 vcc, v2, v6
	s_orn2_b64 s[24:25], vcc, exec
	s_branch .LBB0_1403

; __device__ __forceinline__ unsigned xb_add(unsigned* p, unsigned v) { return __hip_atomic_fetch_add(p, v, __ATOMIC_RELAXED, __HIP_MEMORY_SCOPE_AGENT); }
; __device__ __forceinline__ void xcd_barrier(const XcdBarrier& b) {
;     ...
;             __builtin_amdgcn_fence(__ATOMIC_ACQUIRE, "agent");
;             xb_add(&bar[XB_XGEN(b.x)], 1u);
;             asm volatile("s_waitcnt vmcnt(0)" ::: "memory");
.LBB0_1414:
	s_or_b64 exec, exec, s[6:7]
	s_mov_b64 s[6:7], exec
	v_mbcnt_lo_u32_b32 v1, s6, 0
	v_mbcnt_hi_u32_b32 v1, s7, v1
	v_cmp_eq_u32_e32 vcc, 0, v1
	s_waitcnt vmcnt(0)
	buffer_inv sc1
	s_and_saveexec_b64 s[8:9], vcc
	s_cbranch_execz .LBB0_1416
	s_bcnt1_i32_b64 s6, s[6:7]
	v_mov_b32_e32 v1, 0x2000
	v_mov_b32_e32 v2, s6
.LBB0_1416:
	s_or_b64 exec, exec, s[8:9]
	s_waitcnt vmcnt(0)

; __device__ __forceinline__ unsigned xb_ld(unsigned* p)              { return __hip_atomic_load(p, __ATOMIC_RELAXED, __HIP_MEMORY_SCOPE_AGENT); }
; __device__ __forceinline__ unsigned xb_add(unsigned* p, unsigned v) { return __hip_atomic_fetch_add(p, v, __ATOMIC_RELAXED, __HIP_MEMORY_SCOPE_AGENT); }
; #define XB_SPIN(cond, bar) do { unsigned _sp = 0; while (cond) { __builtin_amdgcn_s_sleep(1); \
;     if ((++_sp & 255u) == 0u) { if (xb_ld(&(bar)[XB_TMO])) break; if (_sp > XB_SPIN_CAP) { atomicAdd(&(bar)[XB_TMO], 1u); break; } } } } while (0)
; __device__ __forceinline__ void xcd_barrier(const XcdBarrier& b) {
;     ...
;         const unsigned old = xb_add(&bar[XB_XSUB(b.x)], 1u);
;         const unsigned gen = old / nloc;
;         if (old + 1u == (gen + 1u) * nloc) {
;     ...
;         } else {
;             XB_SPIN(xb_ld(&bar[XB_XGEN(b.x)]) == gen, bar);
.LBB0_1506:
	s_or_b64 exec, exec, s[8:9]
	v_cvt_f32_u32_e32 v5, v3
	s_waitcnt vmcnt(0)
	v_readfirstlane_b32 s6, v4
	v_sub_u32_e32 v4, 0, v3
	v_rcp_iflag_f32_e32 v5, v5
	v_add_u32_e32 v6, s6, v2
	v_mul_f32_e32 v5, 0x4f7ffffe, v5
	v_cvt_u32_f32_e32 v5, v5
	v_mul_lo_u32 v2, v4, v5
	v_mul_hi_u32 v2, v5, v2
	v_add_u32_e32 v2, v5, v2
	v_mul_hi_u32 v2, v6, v2
	v_mul_lo_u32 v4, v2, v3
	v_sub_u32_e32 v4, v6, v4
	v_add_u32_e32 v5, 1, v2
	v_cmp_ge_u32_e32 vcc, v4, v3
	s_nop 1
	v_cndmask_b32_e32 v2, v2, v5, vcc
	v_sub_u32_e32 v5, v4, v3
	v_cndmask_b32_e32 v4, v4, v5, vcc
	v_add_u32_e32 v5, 1, v2
	v_cmp_ge_u32_e32 vcc, v4, v3
	v_add_u32_e32 v4, 1, v6
	s_nop 0
	v_cndmask_b32_e32 v2, v2, v5, vcc
	v_mul_lo_u32 v5, v3, v2
	v_add_u32_e32 v3, v5, v3
	v_cmp_ne_u32_e32 vcc, v4, v3
	s_and_saveexec_b64 s[6:7], vcc
	s_xor_b64 s[6:7], exec, s[6:7]
	s_cbranch_execz .LBB0_1520
	s_waitcnt lgkmcnt(0)
	v_add_u32_e32 v6, 1, v2
	v_mul_lo_u32 v6, v6, v1
	s_add_u32 s98, s88, 0x7400
	s_addc_u32 s99, s89, 0
	v_mov_b32_e32 v1, 0
	global_load_dword v1, v1, s[98:99] sc1
	s_add_u32 s12, s4, 0x2400
	s_addc_u32 s13, s5, 0
	s_waitcnt vmcnt(0)
	v_cmp_lt_u32_e32 vcc, v1, v6
	s_and_saveexec_b64 s[8:9], vcc
	s_cbranch_execz .LBB0_1519
	s_add_u32 s10, s88, 0x4200
	s_addc_u32 s11, s89, 0
	s_mov_b32 s26, 1
	s_mov_b64 s[14:15], 0
	v_mov_b32_e32 v1, 0
	s_branch .LBB0_1510

; __device__ __forceinline__ unsigned xb_ld(unsigned* p)              { return __hip_atomic_load(p, __ATOMIC_RELAXED, __HIP_MEMORY_SCOPE_AGENT); }
; __device__ __forceinline__ unsigned xb_add(unsigned* p, unsigned v) { return __hip_atomic_fetch_add(p, v, __ATOMIC_RELAXED, __HIP_MEMORY_SCOPE_AGENT); }
; #define XB_SPIN(cond, bar) do { unsigned _sp = 0; while (cond) { __builtin_amdgcn_s_sleep(1); \
;     if ((++_sp & 255u) == 0u) { if (xb_ld(&(bar)[XB_TMO])) break; if (_sp > XB_SPIN_CAP) { atomicAdd(&(bar)[XB_TMO], 1u); break; } } } } while (0)
; __device__ __forceinline__ void xcd_barrier(const XcdBarrier& b) {
;     ...
;             const unsigned og = xb_add(&bar[XB_TOP], 1u);
;             const unsigned tg = og / nx;
;             if (og + 1u == (tg + 1u) * nx) xb_add(&bar[XB_TOPGEN], 1u);
;             else XB_SPIN(xb_ld(&bar[XB_TOPGEN]) == tg, bar);
.LBB0_1523:
	s_or_b64 exec, exec, s[8:9]
	v_cvt_f32_u32_e32 v4, v1
	s_waitcnt vmcnt(0)
	v_readfirstlane_b32 s6, v3
	s_add_u32 s8, s88, 0x7500
	s_addc_u32 s9, s89, 0
	v_rcp_iflag_f32_e32 v4, v4
	v_add_u32_e32 v2, s6, v2
	v_add_u32_e32 v5, 1, v2
	s_mov_b64 s[10:11], -1
	v_mul_f32_e32 v3, 0x4f7ffffe, v4
	v_cvt_u32_f32_e32 v3, v3
	v_sub_u32_e32 v4, 0, v1
	v_mul_lo_u32 v4, v4, v3
	v_mul_hi_u32 v4, v3, v4
	v_add_u32_e32 v3, v3, v4
	v_mul_hi_u32 v3, v2, v3
	v_mul_lo_u32 v4, v3, v1
	v_sub_u32_e32 v2, v2, v4
	v_add_u32_e32 v6, 1, v3
	v_cmp_ge_u32_e32 vcc, v2, v1
	v_sub_u32_e32 v4, v2, v1
	s_nop 0
	v_cndmask_b32_e32 v3, v3, v6, vcc
	v_cndmask_b32_e32 v2, v2, v4, vcc
	v_add_u32_e32 v4, 1, v3
	v_cmp_ge_u32_e32 vcc, v2, v1
	s_nop 1
	v_cndmask_b32_e32 v4, v3, v4, vcc
	v_mul_lo_u32 v2, v1, v4
	v_add_u32_e32 v1, v2, v1
	v_cmp_ne_u32_e32 vcc, v5, v1
	v_mov_b64_e32 v[2:3], s[8:9]
	s_and_saveexec_b64 s[6:7], vcc
	s_cbranch_execz .LBB0_1535
	v_mov_b32_e32 v6, v1
	s_add_u32 s98, s88, 0x7400
	s_addc_u32 s99, s89, 0
	v_mov_b32_e32 v1, 0
	global_load_dword v2, v1, s[98:99] sc1
	s_mov_b64 s[14:15], 0
	s_waitcnt vmcnt(0)
	v_cmp_lt_u32_e32 vcc, v2, v6
	s_and_saveexec_b64 s[12:13], vcc
	s_cbranch_execz .LBB0_1534
	s_add_u32 s10, s88, 0x4200
	s_addc_u32 s11, s89, 0
	s_mov_b32 s26, 1
	s_branch .LBB0_1527

; __device__ __forceinline__ unsigned xb_add(unsigned* p, unsigned v) { return __hip_atomic_fetch_add(p, v, __ATOMIC_RELAXED, __HIP_MEMORY_SCOPE_AGENT); }
; __device__ __forceinline__ void xcd_barrier(const XcdBarrier& b) {
;     ...
;             __builtin_amdgcn_fence(__ATOMIC_ACQUIRE, "agent");
;             xb_add(&bar[XB_XGEN(b.x)], 1u);
;             asm volatile("s_waitcnt vmcnt(0)" ::: "memory");
.LBB0_1537:
	s_or_b64 exec, exec, s[6:7]
	s_mov_b64 s[6:7], exec
	v_mbcnt_lo_u32_b32 v1, s6, 0
	v_mbcnt_hi_u32_b32 v1, s7, v1
	v_cmp_eq_u32_e32 vcc, 0, v1
	s_waitcnt vmcnt(0)
	buffer_inv sc1
	s_and_saveexec_b64 s[8:9], vcc
	s_cbranch_execz .LBB0_1539
	s_bcnt1_i32_b64 s6, s[6:7]
	v_mov_b32_e32 v1, 0x2000
	v_mov_b32_e32 v2, s6
.LBB0_1539:
	s_or_b64 exec, exec, s[8:9]
	s_waitcnt vmcnt(0)
